# E4: E2 + static s_setprio 1 for waves 4-7 during the NSA/GLA-C phase
# speedup vs baseline: 1.0004x; 1.0003x over previous
.LBB0_500:
	s_or_b64 exec, exec, s[0:1]
	v_mov_b32_e32 v2, v226
	s_waitcnt lgkmcnt(0)
	s_barrier
	s_movk_i32 s0, 0x400
	v_readfirstlane_b32 s10, v2
	s_nop 3
	s_cmpk_lt_u32 s10, 0x100
	s_cbranch_scc1 .Lnsa_prio_done
	s_setprio 1
.Lnsa_prio_done:
	s_nop 0
	v_cmp_gt_i32_e32 vcc, s0, v2
	s_and_saveexec_b64 s[0:1], vcc
	v_readlane_b32 s12, v252, 32
	v_readlane_b32 s13, v252, 33
	v_readlane_b32 s14, v252, 34
	v_readlane_b32 s15, v252, 35
	v_readlane_b32 s16, v252, 36
	v_readlane_b32 s17, v252, 37
	v_readlane_b32 s18, v252, 38
	v_readlane_b32 s19, v252, 39
	v_readlane_b32 s20, v252, 40
	v_readlane_b32 s21, v252, 41
	v_readlane_b32 s22, v252, 42
	v_readlane_b32 s23, v252, 43
	v_readlane_b32 s24, v252, 44
	v_readlane_b32 s25, v252, 45
	v_readlane_b32 s26, v252, 46
	v_readlane_b32 s27, v252, 47
	s_cbranch_execz .LBB0_513
	v_and_b32_e32 v0, 0x7f, v2
	s_getpc_b64 s[2:3]
	s_add_u32 s2, s2, _ZL7kBucket@rel32@lo+4
	s_addc_u32 s3, s3, _ZL7kBucket@rel32@hi+12
	global_load_ubyte v0, v0, s[2:3]
	v_max_i32_e32 v1, 0x200, v2
	v_sub_u32_e32 v1, v1, v2
	s_movk_i32 s2, 0x1ff
	v_add_u32_e32 v4, 0x1ff, v1
	s_mov_b64 s[4:5], -1
	v_cmp_lt_u32_e32 vcc, s2, v4
	v_mov_b32_e32 v3, v2
	s_waitcnt vmcnt(0)
	v_lshlrev_b32_e32 v1, 3, v0
	s_and_saveexec_b64 s[2:3], vcc
	s_cbranch_execz .LBB0_510
	v_lshrrev_b32_e32 v6, 9, v4
	v_add_u32_e32 v0, -1, v6
	v_add_u32_e32 v3, 0x200, v2
	v_lshrrev_b32_e32 v4, 1, v0
	v_add_u32_e32 v7, 1, v4
	v_cmp_lt_u32_e32 vcc, 5, v0
	v_mov_b32_e32 v10, 0
	v_mov_b64_e32 v[4:5], v[2:3]
	s_and_saveexec_b64 s[4:5], vcc
	s_cbranch_execz .LBB0_506
	v_readlane_b32 s12, v252, 32
	v_readlane_b32 s13, v252, 33
	v_readlane_b32 s14, v252, 34
	v_readlane_b32 s15, v252, 35
	v_readlane_b32 s20, v252, 40
	v_readlane_b32 s21, v252, 41
	v_lshl_add_u32 v0, v2, 2, 0
	v_readlane_b32 s22, v252, 42
	v_readlane_b32 s23, v252, 43
	s_mov_b64 s[12:13], s[20:21]
	v_and_b32_e32 v8, -4, v7
	s_mov_b32 s9, 0
	v_add_u32_e32 v9, 0x10000, v0
	s_mov_b64 s[6:7], 0
	s_mov_b32 s8, 0x3fb8aa3b
	v_mov_b64_e32 v[4:5], v[2:3]
	s_mov_b64 s[14:15], s[22:23]
	v_readlane_b32 s16, v252, 36
	v_readlane_b32 s17, v252, 37
	v_readlane_b32 s18, v252, 38
	v_readlane_b32 s19, v252, 39
	v_readlane_b32 s24, v252, 44
	v_readlane_b32 s25, v252, 45
	v_readlane_b32 s26, v252, 46
	v_readlane_b32 s27, v252, 47
